# indexer: row-tile epilogues interleaved into the other tile's MFMA chain, software-pipelined across stages; head weights loaded once per unit
# speedup vs baseline: 1.0077x; 1.0017x over previous
.LBB0_699:
	s_mov_b32 s98, 0
	s_lshl_b32 s4, s37, 12
	s_and_b32 s20, s4, 0x7000
	v_add_u32_e32 v0, s20, v124
	v_ashrrev_i32_e32 v1, 31, v0
	v_readlane_b32 s4, v252, 52
	v_lshlrev_b64 v[0:1], 8, v[0:1]
	s_add_i32 s35, s4, 0
	v_lshl_add_u64 v[122:123], v[114:115], 0, v[0:1]
	s_add_i32 m0, s35, 0x10400
	s_mov_b64 s[4:5], 0x2000
	s_barrier
	global_load_lds_dwordx4 v[122:123], off
	v_lshl_add_u64 v[0:1], v[122:123], 0, s[4:5]
	s_add_i32 m0, s35, 0x12400
	s_mov_b64 s[4:5], 0x4000
	global_load_lds_dwordx4 v[0:1], off
	v_lshl_add_u64 v[0:1], v[122:123], 0, s[4:5]
	s_add_i32 m0, s35, 0x14400
	s_mov_b64 s[4:5], 0x6000
	global_load_lds_dwordx4 v[0:1], off
	v_lshl_add_u64 v[0:1], v[122:123], 0, s[4:5]
	s_add_i32 m0, s35, 0x16400
	s_waitcnt lgkmcnt(0)
	s_and_b32 s46, s37, -8
	global_load_lds_dwordx4 v[0:1], off
	s_add_i32 s20, s20, s46
	s_and_saveexec_b64 s[4:5], s[6:7]
	s_cbranch_execz .LBB0_701
	v_add_u32_e32 v0, s20, v137
	v_ashrrev_i32_e32 v1, 31, v0
	v_lshlrev_b64 v[0:1], 6, v[0:1]
	v_lshl_add_u64 v[0:1], v[120:121], 0, v[0:1]
	global_load_dword v0, v[0:1], off
	s_waitcnt vmcnt(0)
	ds_write_b32 v138, v0

.LBB0_704:
	v_readlane_b32 s31, v254, 54
	s_cmp_ge_i32 s31, s21
	v_readlane_b32 s31, v252, 50
	s_nop 1
	v_add_u32_e32 v145, s31, v136
	v_readlane_b32 s31, v252, 51
	s_nop 1
	v_add_u32_e32 v146, s31, v136
	ds_read_b128 v[148:151], v145
	ds_read_b128 v[186:189], v146
	ds_read_b128 v[152:155], v145 offset:16
	ds_read_b128 v[190:193], v146 offset:16
	ds_read_b128 v[156:159], v145 offset:32
	ds_read_b128 v[194:197], v146 offset:32
	ds_read_b128 v[166:169], v145 offset:48
	ds_read_b128 v[198:201], v146 offset:48
	s_waitcnt lgkmcnt(0)
	s_cbranch_scc1 .LBB0_706
	v_add_u32_e32 v0, v127, v128
	ds_read_b128 v[108:111], v0
	v_add_u32_e32 v0, v127, v129
	ds_read_b128 v[104:107], v0
	v_add_u32_e32 v0, v127, v130
	ds_read_b128 v[100:103], v0
	v_add_u32_e32 v0, v127, v131
	ds_read_b128 v[96:99], v0
	v_add_u32_e32 v0, v127, v132
	ds_read_b128 v[92:95], v0
	v_add_u32_e32 v0, v127, v133
	ds_read_b128 v[88:91], v0
	v_add_u32_e32 v0, v127, v134
	ds_read_b128 v[80:83], v0
	v_add_u32_e32 v0, v127, v135
	ds_read_b128 v[84:87], v0
	s_waitcnt lgkmcnt(0)
	v_mfma_f32_32x32x16_bf16 v[0:15], v[16:19], v[108:111], 0
	v_mfma_f32_32x32x16_bf16 v[0:15], v[24:27], v[104:107], v[0:15]
	v_mfma_f32_32x32x16_bf16 v[0:15], v[32:35], v[100:103], v[0:15]
	v_mfma_f32_32x32x16_bf16 v[0:15], v[40:43], v[96:99], v[0:15]
	v_mfma_f32_32x32x16_bf16 v[0:15], v[48:51], v[92:95], v[0:15]
	v_mfma_f32_32x32x16_bf16 v[0:15], v[56:59], v[88:91], v[0:15]
	v_mfma_f32_32x32x16_bf16 v[0:15], v[64:67], v[80:83], v[0:15]
	v_mfma_f32_32x32x16_bf16 v[0:15], v[72:75], v[84:87], v[0:15]
	v_mfma_f32_32x32x16_bf16 v[170:185], v[20:23], v[108:111], 0
	v_mfma_f32_32x32x16_bf16 v[170:185], v[28:31], v[104:107], v[170:185]
	v_mfma_f32_32x32x16_bf16 v[170:185], v[36:39], v[100:103], v[170:185]
	s_nop 8
	v_max_i32_e32 v2, 0, v2
	v_max_i32_e32 v0, 0, v0
	v_mul_f32_e32 v2, v150, v2
	v_fmac_f32_e32 v2, v148, v0
	v_add_f32_e32 v0, 0, v2
	v_max_i32_e32 v2, 0, v3
	v_max_i32_e32 v1, 0, v1
	v_mfma_f32_32x32x16_bf16 v[170:185], v[44:47], v[96:99], v[170:185]
	v_mul_f32_e32 v2, v151, v2
	v_fmac_f32_e32 v2, v149, v1
	v_max_i32_e32 v3, 0, v6
	v_add_f32_e32 v1, 0, v2
	v_max_i32_e32 v2, 0, v4
	v_mul_f32_e32 v3, v154, v3
	v_fmac_f32_e32 v3, v152, v2
	v_mfma_f32_32x32x16_bf16 v[170:185], v[52:55], v[92:95], v[170:185]
	v_add_f32_e32 v0, v3, v0
	v_max_i32_e32 v3, 0, v7
	v_max_i32_e32 v2, 0, v5
	v_mul_f32_e32 v3, v155, v3
	v_fmac_f32_e32 v3, v153, v2
	v_add_f32_e32 v1, v3, v1
	v_max_i32_e32 v3, 0, v10
	v_mfma_f32_32x32x16_bf16 v[170:185], v[60:63], v[88:91], v[170:185]
	v_max_i32_e32 v2, 0, v8
	v_mul_f32_e32 v3, v158, v3
	v_fmac_f32_e32 v3, v156, v2
	v_add_f32_e32 v0, v3, v0
	v_max_i32_e32 v3, 0, v11
	v_max_i32_e32 v2, 0, v9
	v_mul_f32_e32 v3, v159, v3
	v_fmac_f32_e32 v3, v157, v2
	v_mfma_f32_32x32x16_bf16 v[170:185], v[68:71], v[80:83], v[170:185]
	v_add_f32_e32 v1, v3, v1
	v_max_i32_e32 v3, 0, v14
	v_max_i32_e32 v2, 0, v12
	v_mul_f32_e32 v3, v168, v3
	v_fmac_f32_e32 v3, v166, v2
	v_add_f32_e32 v0, v3, v0
	v_max_i32_e32 v3, 0, v15
	v_mfma_f32_32x32x16_bf16 v[170:185], v[76:79], v[84:87], v[170:185]
	v_max_i32_e32 v2, 0, v13
	v_mul_f32_e32 v3, v169, v3
	v_fmac_f32_e32 v3, v167, v2
	v_add_f32_e32 v1, v3, v1
	v_add_f32_e32 v0, v0, v1
	v_cvt_f16_f32_e32 v0, v0
	ds_write_b16 v144, v0
	s_mov_b32 s98, 1
.LBB0_706:
	v_mov_b32_e32 v147, v143
	s_andn2_b64 vcc, exec, s[4:5]
	s_cbranch_vccnz .LBB0_713
	s_mov_b32 s31, 1
	s_mov_b32 s34, 0x8000
	s_movk_i32 s4, 0x160
	v_readlane_b32 s35, v254, 55
	v_mov_b32_e32 v147, v143
	s_branch .LBB0_709

.LBB0_711:
	s_cmp_ge_i32 s35, s21
	s_cbranch_scc1 .Lidx_skipdrain
	s_and_b32 s5, s34, 0x8000
	v_add_u32_e32 v0, s5, v127
	v_add_u32_e32 v1, v0, v128
	ds_read_b128 v[108:111], v1
	v_add_u32_e32 v1, v0, v129
	ds_read_b128 v[104:107], v1
	v_add_u32_e32 v1, v0, v130
	ds_read_b128 v[100:103], v1
	v_add_u32_e32 v1, v0, v131
	ds_read_b128 v[96:99], v1
	v_add_u32_e32 v1, v0, v132
	ds_read_b128 v[92:95], v1
	v_add_u32_e32 v1, v0, v133
	ds_read_b128 v[88:91], v1
	v_add_u32_e32 v1, v0, v134
	v_add_u32_e32 v0, v0, v135
	ds_read_b128 v[80:83], v1
	ds_read_b128 v[84:87], v0
	s_waitcnt lgkmcnt(0)
	v_mfma_f32_32x32x16_bf16 v[0:15], v[16:19], v[108:111], 0
	v_max_i32_e32 v172, 0, v172
	v_max_i32_e32 v170, 0, v170
	v_mul_f32_e32 v172, v188, v172
	v_fmac_f32_e32 v172, v186, v170
	v_add_f32_e32 v170, 0, v172
	v_mfma_f32_32x32x16_bf16 v[0:15], v[24:27], v[104:107], v[0:15]
	v_max_i32_e32 v172, 0, v173
	v_max_i32_e32 v171, 0, v171
	v_mul_f32_e32 v172, v189, v172
	v_fmac_f32_e32 v172, v187, v171
	v_max_i32_e32 v173, 0, v176
	v_mfma_f32_32x32x16_bf16 v[0:15], v[32:35], v[100:103], v[0:15]
	v_add_f32_e32 v171, 0, v172
	v_max_i32_e32 v172, 0, v174
	v_mul_f32_e32 v173, v192, v173
	v_fmac_f32_e32 v173, v190, v172
	v_add_f32_e32 v170, v173, v170
	v_mfma_f32_32x32x16_bf16 v[0:15], v[40:43], v[96:99], v[0:15]
	v_max_i32_e32 v173, 0, v177
	v_max_i32_e32 v172, 0, v175
	v_mul_f32_e32 v173, v193, v173
	v_fmac_f32_e32 v173, v191, v172
	v_add_f32_e32 v171, v173, v171
	v_max_i32_e32 v173, 0, v180
	v_mfma_f32_32x32x16_bf16 v[0:15], v[48:51], v[92:95], v[0:15]
	v_max_i32_e32 v172, 0, v178
	v_mul_f32_e32 v173, v196, v173
	v_fmac_f32_e32 v173, v194, v172
	v_add_f32_e32 v170, v173, v170
	v_max_i32_e32 v173, 0, v181
	v_max_i32_e32 v172, 0, v179
	v_mfma_f32_32x32x16_bf16 v[0:15], v[56:59], v[88:91], v[0:15]
	v_mul_f32_e32 v173, v197, v173
	v_fmac_f32_e32 v173, v195, v172
	v_add_f32_e32 v171, v173, v171
	v_max_i32_e32 v173, 0, v184
	v_max_i32_e32 v172, 0, v182
	v_mul_f32_e32 v173, v200, v173
	v_mfma_f32_32x32x16_bf16 v[0:15], v[64:67], v[80:83], v[0:15]
	v_fmac_f32_e32 v173, v198, v172
	v_add_f32_e32 v170, v173, v170
	v_max_i32_e32 v173, 0, v185
	v_max_i32_e32 v172, 0, v183
	v_mul_f32_e32 v173, v201, v173
	v_mfma_f32_32x32x16_bf16 v[0:15], v[72:75], v[84:87], v[0:15]
	v_fmac_f32_e32 v173, v199, v172
	v_add_f32_e32 v171, v173, v171
	v_add_f32_e32 v170, v170, v171
	v_cvt_f16_f32_e32 v170, v170
	ds_write_b16 v147, v170 offset:16128
	v_mfma_f32_32x32x16_bf16 v[170:185], v[20:23], v[108:111], 0
	v_mfma_f32_32x32x16_bf16 v[170:185], v[28:31], v[104:107], v[170:185]
	v_mfma_f32_32x32x16_bf16 v[170:185], v[36:39], v[100:103], v[170:185]
	s_nop 3
	v_max_i32_e32 v2, 0, v2
	v_max_i32_e32 v0, 0, v0
	v_mul_f32_e32 v2, v150, v2
	v_fmac_f32_e32 v2, v148, v0
	v_add_f32_e32 v0, 0, v2
	v_max_i32_e32 v2, 0, v3
	v_max_i32_e32 v1, 0, v1
	v_mfma_f32_32x32x16_bf16 v[170:185], v[44:47], v[96:99], v[170:185]
	v_mul_f32_e32 v2, v151, v2
	v_fmac_f32_e32 v2, v149, v1
	v_max_i32_e32 v3, 0, v6
	v_add_f32_e32 v1, 0, v2
	v_max_i32_e32 v2, 0, v4
	v_mul_f32_e32 v3, v154, v3
	v_fmac_f32_e32 v3, v152, v2
	v_mfma_f32_32x32x16_bf16 v[170:185], v[52:55], v[92:95], v[170:185]
	v_add_f32_e32 v0, v3, v0
	v_max_i32_e32 v3, 0, v7
	v_max_i32_e32 v2, 0, v5
	v_mul_f32_e32 v3, v155, v3
	v_fmac_f32_e32 v3, v153, v2
	v_add_f32_e32 v1, v3, v1
	v_max_i32_e32 v3, 0, v10
	v_mfma_f32_32x32x16_bf16 v[170:185], v[60:63], v[88:91], v[170:185]
	v_max_i32_e32 v2, 0, v8
	v_mul_f32_e32 v3, v158, v3
	v_fmac_f32_e32 v3, v156, v2
	v_add_f32_e32 v0, v3, v0
	v_max_i32_e32 v3, 0, v11
	v_max_i32_e32 v2, 0, v9
	v_mul_f32_e32 v3, v159, v3
	v_fmac_f32_e32 v3, v157, v2
	v_mfma_f32_32x32x16_bf16 v[170:185], v[68:71], v[80:83], v[170:185]
	v_add_f32_e32 v1, v3, v1
	v_max_i32_e32 v3, 0, v14
	v_max_i32_e32 v2, 0, v12
	v_mul_f32_e32 v3, v168, v3
	v_fmac_f32_e32 v3, v166, v2
	v_add_f32_e32 v0, v3, v0
	v_max_i32_e32 v3, 0, v15
	v_mfma_f32_32x32x16_bf16 v[170:185], v[76:79], v[84:87], v[170:185]
	v_max_i32_e32 v2, 0, v13
	v_mul_f32_e32 v3, v169, v3
	v_fmac_f32_e32 v3, v167, v2
	v_add_f32_e32 v1, v3, v1
	v_add_f32_e32 v0, v0, v1
	v_cvt_f16_f32_e32 v0, v0
	ds_write_b16 v147, v0
	s_branch .LBB0_708
.Lidx_skipdrain:
	s_cmp_eq_u32 s98, 0
	s_cbranch_scc1 .LBB0_708
	s_nop 3
	v_max_i32_e32 v172, 0, v172
	v_max_i32_e32 v170, 0, v170
	v_mul_f32_e32 v172, v188, v172
	v_fmac_f32_e32 v172, v186, v170
	v_add_f32_e32 v170, 0, v172
	v_max_i32_e32 v172, 0, v173
	v_max_i32_e32 v171, 0, v171
	v_mul_f32_e32 v172, v189, v172
	v_fmac_f32_e32 v172, v187, v171
	v_max_i32_e32 v173, 0, v176
	v_add_f32_e32 v171, 0, v172
	v_max_i32_e32 v172, 0, v174
	v_mul_f32_e32 v173, v192, v173
	v_fmac_f32_e32 v173, v190, v172
	v_add_f32_e32 v170, v173, v170
	v_max_i32_e32 v173, 0, v177
	v_max_i32_e32 v172, 0, v175
	v_mul_f32_e32 v173, v193, v173
	v_fmac_f32_e32 v173, v191, v172
	v_add_f32_e32 v171, v173, v171
	v_max_i32_e32 v173, 0, v180
	v_max_i32_e32 v172, 0, v178
	v_mul_f32_e32 v173, v196, v173
	v_fmac_f32_e32 v173, v194, v172
	v_add_f32_e32 v170, v173, v170
	v_max_i32_e32 v173, 0, v181
	v_max_i32_e32 v172, 0, v179
	v_mul_f32_e32 v173, v197, v173
	v_fmac_f32_e32 v173, v195, v172
	v_add_f32_e32 v171, v173, v171
	v_max_i32_e32 v173, 0, v184
	v_max_i32_e32 v172, 0, v182
	v_mul_f32_e32 v173, v200, v173
	v_fmac_f32_e32 v173, v198, v172
	v_add_f32_e32 v170, v173, v170
	v_max_i32_e32 v173, 0, v185
	v_max_i32_e32 v172, 0, v183
	v_mul_f32_e32 v173, v201, v173
	v_fmac_f32_e32 v173, v199, v172
	v_add_f32_e32 v171, v173, v171
	v_add_f32_e32 v170, v170, v171
	v_cvt_f16_f32_e32 v170, v170
	ds_write_b16 v147, v170 offset:16128
	s_mov_b32 s98, 0
	s_branch .LBB0_708
.LBB0_713:
	s_cmp_eq_u32 s98, 0
	s_cbranch_scc1 .Lidx_nodrain
	s_nop 3
	v_max_i32_e32 v172, 0, v172
	v_max_i32_e32 v170, 0, v170
	v_mul_f32_e32 v172, v188, v172
	v_fmac_f32_e32 v172, v186, v170
	v_add_f32_e32 v170, 0, v172
	v_max_i32_e32 v172, 0, v173
	v_max_i32_e32 v171, 0, v171
	v_mul_f32_e32 v172, v189, v172
	v_fmac_f32_e32 v172, v187, v171
	v_max_i32_e32 v173, 0, v176
	v_add_f32_e32 v171, 0, v172
	v_max_i32_e32 v172, 0, v174
	v_mul_f32_e32 v173, v192, v173
	v_fmac_f32_e32 v173, v190, v172
	v_add_f32_e32 v170, v173, v170
	v_max_i32_e32 v173, 0, v177
	v_max_i32_e32 v172, 0, v175
	v_mul_f32_e32 v173, v193, v173
	v_fmac_f32_e32 v173, v191, v172
	v_add_f32_e32 v171, v173, v171
	v_max_i32_e32 v173, 0, v180
	v_max_i32_e32 v172, 0, v178
	v_mul_f32_e32 v173, v196, v173
	v_fmac_f32_e32 v173, v194, v172
	v_add_f32_e32 v170, v173, v170
	v_max_i32_e32 v173, 0, v181
	v_max_i32_e32 v172, 0, v179
	v_mul_f32_e32 v173, v197, v173
	v_fmac_f32_e32 v173, v195, v172
	v_add_f32_e32 v171, v173, v171
	v_max_i32_e32 v173, 0, v184
	v_max_i32_e32 v172, 0, v182
	v_mul_f32_e32 v173, v200, v173
	v_fmac_f32_e32 v173, v198, v172
	v_add_f32_e32 v170, v173, v170
	v_max_i32_e32 v173, 0, v185
	v_max_i32_e32 v172, 0, v183
	v_mul_f32_e32 v173, v201, v173
	v_fmac_f32_e32 v173, v199, v172
	v_add_f32_e32 v171, v173, v171
	v_add_f32_e32 v170, v170, v171
	v_cvt_f16_f32_e32 v170, v170
	ds_write_b16 v147, v170 offset:16128
